# c22
# speedup vs baseline: 1.0011x; 1.0005x over previous
.LBB1_3:
	s_and_b32 s8, s55, 6
	ds_read_b128 v[114:117], v77
	ds_read_b128 v[118:121], v77 offset:512
	ds_read_b128 v[122:125], v77 offset:1024
	ds_read_b128 v[126:129], v77 offset:1536
	ds_read_b64 v[90:91], v78
	ds_read_b64 v[92:93], v78 offset:8
	ds_read_b64 v[94:95], v78 offset:16
	ds_read_b64 v[96:97], v81
	ds_read_b64 v[98:99], v81 offset:8
	ds_read_b64 v[100:101], v81 offset:16
	v_lshl_add_u32 v89, s8, 9, v87
	ds_read_u16 v154, v89
	ds_read_b128 v[130:133], v77 offset:8192
	ds_read_b128 v[134:137], v77 offset:8704
	ds_read_b128 v[138:141], v77 offset:9216
	ds_read_b128 v[142:145], v77 offset:9728
	ds_read_b64 v[102:103], v80
	ds_read_b64 v[104:105], v80 offset:8
	ds_read_b64 v[106:107], v80 offset:16
	s_mov_b32 m0, s50
	ds_read_b64 v[108:109], v79
	ds_read_b64 v[110:111], v79 offset:8
	ds_read_b64 v[112:113], v79 offset:16
	ds_read_u16 v89, v89 offset:512
	global_load_lds_dwordx4 v161, s[72:73]
	s_mov_b32 m0, s51
	s_add_i32 s56, s37, s55
	global_load_lds_dwordx4 v162, s[72:73]
	s_mov_b32 m0, s52
	s_add_i32 s8, s56, 4
	global_load_lds_dwordx4 v167, s[76:77]
	s_mov_b32 m0, s53
	s_min_u32 s57, s8, 63
	global_load_lds_dwordx4 v168, s[76:77]
	s_mov_b32 m0, s54
	s_lshl_b32 s8, s57, 10
	global_load_lds_dwordx4 v169, s[76:77]
	s_add_u32 s82, s80, s8
	s_addc_u32 s83, s81, 0
	s_lshl_b32 s8, s57, 9
	s_and_b32 s8, s8, 0xe00
	s_add_i32 m0, s49, s8
	s_add_i32 s57, s55, 4
	global_load_lds_dword v160, s[82:83]
	s_sleep 2
	s_waitcnt vmcnt(6)
	s_waitcnt lgkmcnt(0)
	s_barrier
	s_setprio 1
	s_waitcnt lgkmcnt(0)
	v_mfma_scale_f32_32x32x64_f8f6f4 v[50:65], v[90:95], v[114:117], v[50:65], v154, v88 op_sel_hi:[0,0,0] cbsz:2 blgp:4
	v_mfma_scale_f32_32x32x64_f8f6f4 v[34:49], v[90:95], v[118:121], v[34:49], v154, v88 op_sel_hi:[0,0,0] cbsz:2 blgp:4
	v_mfma_scale_f32_32x32x64_f8f6f4 v[18:33], v[90:95], v[122:125], v[18:33], v154, v88 op_sel_hi:[0,0,0] cbsz:2 blgp:4
	v_mfma_scale_f32_32x32x64_f8f6f4 v[2:17], v[90:95], v[126:129], v[2:17], v154, v88 op_sel_hi:[0,0,0] cbsz:2 blgp:4
	v_mfma_scale_f32_32x32x64_f8f6f4 v[50:65], v[96:101], v[114:117], v[50:65], v154, v88 op_sel:[1,0,0] op_sel_hi:[0,0,0] cbsz:2 blgp:4
	v_mfma_scale_f32_32x32x64_f8f6f4 v[34:49], v[96:101], v[118:121], v[34:49], v154, v88 op_sel:[1,0,0] op_sel_hi:[0,0,0] cbsz:2 blgp:4
	v_mfma_scale_f32_32x32x64_f8f6f4 v[18:33], v[96:101], v[122:125], v[18:33], v154, v88 op_sel:[1,0,0] op_sel_hi:[0,0,0] cbsz:2 blgp:4
	v_mfma_scale_f32_32x32x64_f8f6f4 v[2:17], v[96:101], v[126:129], v[2:17], v154, v88 op_sel:[1,0,0] op_sel_hi:[0,0,0] cbsz:2 blgp:4
	v_mfma_scale_f32_32x32x64_f8f6f4 v[50:65], v[102:107], v[130:133], v[50:65], v89, v88 op_sel_hi:[0,0,0] cbsz:2 blgp:4
	v_mfma_scale_f32_32x32x64_f8f6f4 v[34:49], v[102:107], v[134:137], v[34:49], v89, v88 op_sel_hi:[0,0,0] cbsz:2 blgp:4
	v_mfma_scale_f32_32x32x64_f8f6f4 v[18:33], v[102:107], v[138:141], v[18:33], v89, v88 op_sel_hi:[0,0,0] cbsz:2 blgp:4
	v_mfma_scale_f32_32x32x64_f8f6f4 v[2:17], v[102:107], v[142:145], v[2:17], v89, v88 op_sel_hi:[0,0,0] cbsz:2 blgp:4
	v_mfma_scale_f32_32x32x64_f8f6f4 v[50:65], v[108:113], v[130:133], v[50:65], v89, v88 op_sel:[1,0,0] op_sel_hi:[0,0,0] cbsz:2 blgp:4
	v_mfma_scale_f32_32x32x64_f8f6f4 v[34:49], v[108:113], v[134:137], v[34:49], v89, v88 op_sel:[1,0,0] op_sel_hi:[0,0,0] cbsz:2 blgp:4
	v_mfma_scale_f32_32x32x64_f8f6f4 v[18:33], v[108:113], v[138:141], v[18:33], v89, v88 op_sel:[1,0,0] op_sel_hi:[0,0,0] cbsz:2 blgp:4
	v_mfma_scale_f32_32x32x64_f8f6f4 v[2:17], v[108:113], v[142:145], v[2:17], v89, v88 op_sel:[1,0,0] op_sel_hi:[0,0,0] cbsz:2 blgp:4
	s_setprio 0
	s_barrier
	s_add_i32 s8, s55, 2
	s_and_b32 s8, s8, 6
	ds_read_b128 v[114:117], v77 offset:40960
	ds_read_b128 v[118:121], v77 offset:41472
	ds_read_b128 v[122:125], v77 offset:41984
	ds_read_b128 v[126:129], v77 offset:42496
	ds_read_b64 v[90:91], v75
	ds_read_b64 v[92:93], v75 offset:8
	ds_read_b64 v[94:95], v75 offset:16
	ds_read_b64 v[96:97], v76
	ds_read_b64 v[98:99], v76 offset:8
	ds_read_b64 v[100:101], v76 offset:16
	v_lshl_add_u32 v89, s8, 9, v87
	ds_read_u16 v154, v89
	ds_read_b128 v[130:133], v77 offset:49152
	ds_read_b128 v[134:137], v77 offset:49664
	ds_read_b128 v[138:141], v77 offset:50176
	ds_read_b128 v[142:145], v77 offset:50688
	ds_read_b64 v[102:103], v74
	ds_read_b64 v[104:105], v74 offset:8
	ds_read_b64 v[106:107], v74 offset:16
	s_mov_b32 m0, s38
	ds_read_b64 v[108:109], v73
	ds_read_b64 v[110:111], v73 offset:8
	ds_read_b64 v[112:113], v73 offset:16
	ds_read_u16 v89, v89 offset:512
	global_load_lds_dwordx4 v163, s[72:73]
	s_mov_b32 m0, s39
	s_add_i32 s8, s56, 6
	global_load_lds_dwordx4 v164, s[72:73]
	s_mov_b32 m0, s40
	s_min_u32 s58, s8, 63
	global_load_lds_dwordx4 v170, s[76:77]
	s_mov_b32 m0, s41
	s_lshl_b32 s8, s58, 10
	global_load_lds_dwordx4 v171, s[76:77]
	s_mov_b32 m0, s42
	s_nop 0
	global_load_lds_dwordx4 v172, s[76:77]
	s_add_u32 s82, s80, s8
	s_addc_u32 s83, s81, 0
	s_lshl_b32 s8, s58, 9
	s_and_b32 s8, s8, 0xe00
	s_add_i32 m0, s49, s8
	s_nop 0
	global_load_lds_dword v160, s[82:83]
	s_sleep 2
	s_waitcnt vmcnt(6)
	s_waitcnt lgkmcnt(0)
	s_barrier
	s_setprio 1
	s_waitcnt lgkmcnt(0)
	v_mfma_scale_f32_32x32x64_f8f6f4 v[50:65], v[90:95], v[114:117], v[50:65], v154, v88 op_sel_hi:[0,0,0] cbsz:2 blgp:4
	v_mfma_scale_f32_32x32x64_f8f6f4 v[34:49], v[90:95], v[118:121], v[34:49], v154, v88 op_sel_hi:[0,0,0] cbsz:2 blgp:4
	v_mfma_scale_f32_32x32x64_f8f6f4 v[18:33], v[90:95], v[122:125], v[18:33], v154, v88 op_sel_hi:[0,0,0] cbsz:2 blgp:4
	v_mfma_scale_f32_32x32x64_f8f6f4 v[2:17], v[90:95], v[126:129], v[2:17], v154, v88 op_sel_hi:[0,0,0] cbsz:2 blgp:4
	v_mfma_scale_f32_32x32x64_f8f6f4 v[50:65], v[96:101], v[114:117], v[50:65], v154, v88 op_sel:[1,0,0] op_sel_hi:[0,0,0] cbsz:2 blgp:4
	v_mfma_scale_f32_32x32x64_f8f6f4 v[34:49], v[96:101], v[118:121], v[34:49], v154, v88 op_sel:[1,0,0] op_sel_hi:[0,0,0] cbsz:2 blgp:4
	v_mfma_scale_f32_32x32x64_f8f6f4 v[18:33], v[96:101], v[122:125], v[18:33], v154, v88 op_sel:[1,0,0] op_sel_hi:[0,0,0] cbsz:2 blgp:4
	v_mfma_scale_f32_32x32x64_f8f6f4 v[2:17], v[96:101], v[126:129], v[2:17], v154, v88 op_sel:[1,0,0] op_sel_hi:[0,0,0] cbsz:2 blgp:4
	v_mfma_scale_f32_32x32x64_f8f6f4 v[50:65], v[102:107], v[130:133], v[50:65], v89, v88 op_sel_hi:[0,0,0] cbsz:2 blgp:4
	v_mfma_scale_f32_32x32x64_f8f6f4 v[34:49], v[102:107], v[134:137], v[34:49], v89, v88 op_sel_hi:[0,0,0] cbsz:2 blgp:4
	v_mfma_scale_f32_32x32x64_f8f6f4 v[18:33], v[102:107], v[138:141], v[18:33], v89, v88 op_sel_hi:[0,0,0] cbsz:2 blgp:4
	v_mfma_scale_f32_32x32x64_f8f6f4 v[2:17], v[102:107], v[142:145], v[2:17], v89, v88 op_sel_hi:[0,0,0] cbsz:2 blgp:4
	v_mfma_scale_f32_32x32x64_f8f6f4 v[50:65], v[108:113], v[130:133], v[50:65], v89, v88 op_sel:[1,0,0] op_sel_hi:[0,0,0] cbsz:2 blgp:4
	v_mfma_scale_f32_32x32x64_f8f6f4 v[34:49], v[108:113], v[134:137], v[34:49], v89, v88 op_sel:[1,0,0] op_sel_hi:[0,0,0] cbsz:2 blgp:4
	v_mfma_scale_f32_32x32x64_f8f6f4 v[18:33], v[108:113], v[138:141], v[18:33], v89, v88 op_sel:[1,0,0] op_sel_hi:[0,0,0] cbsz:2 blgp:4
	v_mfma_scale_f32_32x32x64_f8f6f4 v[2:17], v[108:113], v[142:145], v[2:17], v89, v88 op_sel:[1,0,0] op_sel_hi:[0,0,0] cbsz:2 blgp:4
	s_setprio 0
	s_barrier
	s_and_b32 s8, s57, 6
	ds_read_b128 v[114:117], v86
	ds_read_b128 v[118:121], v86 offset:512
	ds_read_b128 v[122:125], v86 offset:1024
	ds_read_b128 v[126:129], v86 offset:1536
	ds_read_b64 v[90:91], v82
	ds_read_b64 v[92:93], v82 offset:8
	ds_read_b64 v[94:95], v82 offset:16
	ds_read_b64 v[96:97], v83
	ds_read_b64 v[98:99], v83 offset:8
	ds_read_b64 v[100:101], v83 offset:16
	v_lshl_add_u32 v89, s8, 9, v87
	ds_read_u16 v154, v89
	ds_read_b128 v[130:133], v86 offset:8192
	ds_read_b128 v[134:137], v86 offset:8704
	ds_read_b128 v[138:141], v86 offset:9216
	ds_read_b128 v[142:145], v86 offset:9728
	ds_read_b64 v[102:103], v84
	ds_read_b64 v[104:105], v84 offset:8
	ds_read_b64 v[106:107], v84 offset:16
	s_mov_b32 m0, s43
	ds_read_b64 v[108:109], v85
	ds_read_b64 v[110:111], v85 offset:8
	ds_read_b64 v[112:113], v85 offset:16
	ds_read_u16 v89, v89 offset:512
	global_load_lds_dwordx4 v165, s[72:73]
	s_mov_b32 m0, s44
	s_nop 0
	global_load_lds_dwordx4 v166, s[72:73]
	s_mov_b32 m0, s45
	s_add_i32 s56, s56, 8
	global_load_lds_dwordx4 v173, s[76:77]
	s_mov_b32 m0, s46
	s_min_u32 s56, s56, 63
	global_load_lds_dwordx4 v174, s[76:77]
	s_mov_b32 m0, s47
	s_lshl_b32 s8, s56, 10
	global_load_lds_dwordx4 v175, s[76:77]
	s_add_u32 s82, s80, s8
	s_addc_u32 s83, s81, 0
	s_lshl_b32 s8, s56, 9
	s_and_b32 s8, s8, 0xe00
	s_add_i32 m0, s49, s8
	s_nop 0
	global_load_lds_dword v160, s[82:83]
	s_sleep 2
	s_waitcnt vmcnt(6)
	s_waitcnt lgkmcnt(0)
	s_barrier
	s_setprio 1
	s_waitcnt lgkmcnt(0)
	v_mfma_scale_f32_32x32x64_f8f6f4 v[50:65], v[90:95], v[114:117], v[50:65], v154, v88 op_sel_hi:[0,0,0] cbsz:2 blgp:4
	v_mfma_scale_f32_32x32x64_f8f6f4 v[34:49], v[90:95], v[118:121], v[34:49], v154, v88 op_sel_hi:[0,0,0] cbsz:2 blgp:4
	v_mfma_scale_f32_32x32x64_f8f6f4 v[18:33], v[90:95], v[122:125], v[18:33], v154, v88 op_sel_hi:[0,0,0] cbsz:2 blgp:4
	v_mfma_scale_f32_32x32x64_f8f6f4 v[2:17], v[90:95], v[126:129], v[2:17], v154, v88 op_sel_hi:[0,0,0] cbsz:2 blgp:4
	v_mfma_scale_f32_32x32x64_f8f6f4 v[50:65], v[96:101], v[114:117], v[50:65], v154, v88 op_sel:[1,0,0] op_sel_hi:[0,0,0] cbsz:2 blgp:4
	v_mfma_scale_f32_32x32x64_f8f6f4 v[34:49], v[96:101], v[118:121], v[34:49], v154, v88 op_sel:[1,0,0] op_sel_hi:[0,0,0] cbsz:2 blgp:4
	v_mfma_scale_f32_32x32x64_f8f6f4 v[18:33], v[96:101], v[122:125], v[18:33], v154, v88 op_sel:[1,0,0] op_sel_hi:[0,0,0] cbsz:2 blgp:4
	v_mfma_scale_f32_32x32x64_f8f6f4 v[2:17], v[96:101], v[126:129], v[2:17], v154, v88 op_sel:[1,0,0] op_sel_hi:[0,0,0] cbsz:2 blgp:4
	v_mfma_scale_f32_32x32x64_f8f6f4 v[50:65], v[102:107], v[130:133], v[50:65], v89, v88 op_sel_hi:[0,0,0] cbsz:2 blgp:4
	v_mfma_scale_f32_32x32x64_f8f6f4 v[34:49], v[102:107], v[134:137], v[34:49], v89, v88 op_sel_hi:[0,0,0] cbsz:2 blgp:4
	v_mfma_scale_f32_32x32x64_f8f6f4 v[18:33], v[102:107], v[138:141], v[18:33], v89, v88 op_sel_hi:[0,0,0] cbsz:2 blgp:4
	v_mfma_scale_f32_32x32x64_f8f6f4 v[2:17], v[102:107], v[142:145], v[2:17], v89, v88 op_sel_hi:[0,0,0] cbsz:2 blgp:4
	v_mfma_scale_f32_32x32x64_f8f6f4 v[50:65], v[108:113], v[130:133], v[50:65], v89, v88 op_sel:[1,0,0] op_sel_hi:[0,0,0] cbsz:2 blgp:4
	v_mfma_scale_f32_32x32x64_f8f6f4 v[34:49], v[108:113], v[134:137], v[34:49], v89, v88 op_sel:[1,0,0] op_sel_hi:[0,0,0] cbsz:2 blgp:4
	v_mfma_scale_f32_32x32x64_f8f6f4 v[18:33], v[108:113], v[138:141], v[18:33], v89, v88 op_sel:[1,0,0] op_sel_hi:[0,0,0] cbsz:2 blgp:4
	v_mfma_scale_f32_32x32x64_f8f6f4 v[2:17], v[108:113], v[142:145], v[2:17], v89, v88 op_sel:[1,0,0] op_sel_hi:[0,0,0] cbsz:2 blgp:4
	s_setprio 0
	s_barrier
	s_add_i32 s48, s48, 3
	s_add_i32 s55, s55, 6
	s_add_u32 s72, s72, 0xc000
	s_addc_u32 s73, s73, 0
	s_add_u32 s76, s76, 0x24000
	s_addc_u32 s77, s77, 0
	s_cmp_lt_u32 s48, 27
	s_cbranch_scc1 .LBB1_3
	ds_read_b128 v[66:69], v77
	ds_read_b128 v[106:109], v77 offset:512
	ds_read_b128 v[110:113], v77 offset:1024
	ds_read_b128 v[114:117], v77 offset:1536
	ds_read_b64 v[82:83], v78
	ds_read_b64 v[84:85], v78 offset:8
	ds_read_b64 v[86:87], v78 offset:16
	ds_read_b64 v[88:89], v81
	ds_read_b64 v[90:91], v81 offset:8
	ds_read_b64 v[92:93], v81 offset:16
	v_add_u32_e32 v0, 0x1e800, v72
	ds_read_u16 v0, v0
	ds_read_b128 v[118:121], v77 offset:8192
	ds_read_b128 v[122:125], v77 offset:8704
	ds_read_b128 v[126:129], v77 offset:9216
	ds_read_b128 v[130:133], v77 offset:9728
	ds_read_b64 v[94:95], v80
	ds_read_b64 v[96:97], v80 offset:8
	ds_read_b64 v[98:99], v80 offset:16
	ds_read_b64 v[100:101], v79
	ds_read_b64 v[102:103], v79 offset:8
	ds_read_b64 v[104:105], v79 offset:16
	v_add_u32_e32 v1, 0x1ea00, v72
	ds_read_u16 v1, v1
	s_waitcnt vmcnt(0)
	s_waitcnt lgkmcnt(0)
	s_barrier
	s_setprio 1
	v_mov_b32_e32 v134, 0x7f7f7f7f
	s_waitcnt lgkmcnt(0)
	s_nop 0
	v_mfma_scale_f32_32x32x64_f8f6f4 v[50:65], v[82:87], v[66:69], v[50:65], v0, v134 op_sel_hi:[0,0,0] cbsz:2 blgp:4
	v_mfma_scale_f32_32x32x64_f8f6f4 v[34:49], v[82:87], v[106:109], v[34:49], v0, v134 op_sel_hi:[0,0,0] cbsz:2 blgp:4
	v_mfma_scale_f32_32x32x64_f8f6f4 v[18:33], v[82:87], v[110:113], v[18:33], v0, v134 op_sel_hi:[0,0,0] cbsz:2 blgp:4
	v_mfma_scale_f32_32x32x64_f8f6f4 v[2:17], v[82:87], v[114:117], v[2:17], v0, v134 op_sel_hi:[0,0,0] cbsz:2 blgp:4
	v_mfma_scale_f32_32x32x64_f8f6f4 v[50:65], v[88:93], v[66:69], v[50:65], v0, v134 op_sel:[1,0,0] op_sel_hi:[0,0,0] cbsz:2 blgp:4
	v_mfma_scale_f32_32x32x64_f8f6f4 v[34:49], v[88:93], v[106:109], v[34:49], v0, v134 op_sel:[1,0,0] op_sel_hi:[0,0,0] cbsz:2 blgp:4
	v_mfma_scale_f32_32x32x64_f8f6f4 v[18:33], v[88:93], v[110:113], v[18:33], v0, v134 op_sel:[1,0,0] op_sel_hi:[0,0,0] cbsz:2 blgp:4
	v_mfma_scale_f32_32x32x64_f8f6f4 v[2:17], v[88:93], v[114:117], v[2:17], v0, v134 op_sel:[1,0,0] op_sel_hi:[0,0,0] cbsz:2 blgp:4
	v_lshrrev_b32_e32 v0, 8, v1
	v_mfma_scale_f32_32x32x64_f8f6f4 v[50:65], v[94:99], v[118:121], v[50:65], v1, v134 op_sel_hi:[0,0,0] cbsz:2 blgp:4
	v_mfma_scale_f32_32x32x64_f8f6f4 v[34:49], v[94:99], v[122:125], v[34:49], v1, v134 op_sel_hi:[0,0,0] cbsz:2 blgp:4
	v_mfma_scale_f32_32x32x64_f8f6f4 v[18:33], v[94:99], v[126:129], v[18:33], v1, v134 op_sel_hi:[0,0,0] cbsz:2 blgp:4
	v_mfma_scale_f32_32x32x64_f8f6f4 v[2:17], v[94:99], v[130:133], v[2:17], v1, v134 op_sel_hi:[0,0,0] cbsz:2 blgp:4
	v_mfma_scale_f32_32x32x64_f8f6f4 v[50:65], v[100:105], v[118:121], v[50:65], v0, v134 op_sel_hi:[0,0,0] cbsz:2 blgp:4
	v_mfma_scale_f32_32x32x64_f8f6f4 v[34:49], v[100:105], v[122:125], v[34:49], v0, v134 op_sel_hi:[0,0,0] cbsz:2 blgp:4
	v_mfma_scale_f32_32x32x64_f8f6f4 v[18:33], v[100:105], v[126:129], v[18:33], v0, v134 op_sel_hi:[0,0,0] cbsz:2 blgp:4
	v_mfma_scale_f32_32x32x64_f8f6f4 v[2:17], v[100:105], v[130:133], v[2:17], v0, v134 op_sel_hi:[0,0,0] cbsz:2 blgp:4
	s_setprio 0
	s_barrier
	ds_read_b128 v[66:69], v77 offset:40960
	ds_read_b128 v[102:105], v77 offset:41472
	ds_read_b128 v[106:109], v77 offset:41984
	ds_read_b128 v[110:113], v77 offset:42496
	ds_read_b64 v[78:79], v75
	ds_read_b64 v[80:81], v75 offset:8
	ds_read_b64 v[82:83], v75 offset:16
	ds_read_b64 v[84:85], v76
	ds_read_b64 v[86:87], v76 offset:8
	ds_read_b64 v[88:89], v76 offset:16
	v_add_u32_e32 v0, 0x1ec00, v72
	ds_read_u16 v0, v0
	ds_read_b128 v[114:117], v77 offset:49152
	ds_read_b128 v[118:121], v77 offset:49664
	ds_read_b128 v[122:125], v77 offset:50176
	ds_read_b128 v[126:129], v77 offset:50688
	ds_read_b64 v[90:91], v74
	ds_read_b64 v[92:93], v74 offset:8
	ds_read_b64 v[94:95], v74 offset:16
	ds_read_b64 v[96:97], v73
	ds_read_b64 v[98:99], v73 offset:8
	ds_read_b64 v[100:101], v73 offset:16
	v_add_u32_e32 v1, 0x1ee00, v72
	ds_read_u16 v1, v1
	s_waitcnt vmcnt(0)
	s_waitcnt lgkmcnt(0)
	s_barrier
	s_setprio 1
	s_waitcnt lgkmcnt(0)
	v_mfma_scale_f32_32x32x64_f8f6f4 v[50:65], v[78:83], v[66:69], v[50:65], v0, v134 op_sel_hi:[0,0,0] cbsz:2 blgp:4
	v_mfma_scale_f32_32x32x64_f8f6f4 v[34:49], v[78:83], v[102:105], v[34:49], v0, v134 op_sel_hi:[0,0,0] cbsz:2 blgp:4
	v_mfma_scale_f32_32x32x64_f8f6f4 v[18:33], v[78:83], v[106:109], v[18:33], v0, v134 op_sel_hi:[0,0,0] cbsz:2 blgp:4
	v_mfma_scale_f32_32x32x64_f8f6f4 v[2:17], v[78:83], v[110:113], v[2:17], v0, v134 op_sel_hi:[0,0,0] cbsz:2 blgp:4
	v_mfma_scale_f32_32x32x64_f8f6f4 v[50:65], v[84:89], v[66:69], v[50:65], v0, v134 op_sel:[1,0,0] op_sel_hi:[0,0,0] cbsz:2 blgp:4
	v_mfma_scale_f32_32x32x64_f8f6f4 v[34:49], v[84:89], v[102:105], v[34:49], v0, v134 op_sel:[1,0,0] op_sel_hi:[0,0,0] cbsz:2 blgp:4
	v_mfma_scale_f32_32x32x64_f8f6f4 v[18:33], v[84:89], v[106:109], v[18:33], v0, v134 op_sel:[1,0,0] op_sel_hi:[0,0,0] cbsz:2 blgp:4
	v_mfma_scale_f32_32x32x64_f8f6f4 v[2:17], v[84:89], v[110:113], v[2:17], v0, v134 op_sel:[1,0,0] op_sel_hi:[0,0,0] cbsz:2 blgp:4
	v_lshrrev_b32_e32 v0, 8, v1
	v_mfma_scale_f32_32x32x64_f8f6f4 v[50:65], v[90:95], v[114:117], v[50:65], v1, v134 op_sel_hi:[0,0,0] cbsz:2 blgp:4
	v_mfma_scale_f32_32x32x64_f8f6f4 v[34:49], v[90:95], v[118:121], v[34:49], v1, v134 op_sel_hi:[0,0,0] cbsz:2 blgp:4
	v_mfma_scale_f32_32x32x64_f8f6f4 v[18:33], v[90:95], v[122:125], v[18:33], v1, v134 op_sel_hi:[0,0,0] cbsz:2 blgp:4
	v_mfma_scale_f32_32x32x64_f8f6f4 v[2:17], v[90:95], v[126:129], v[2:17], v1, v134 op_sel_hi:[0,0,0] cbsz:2 blgp:4
	v_mfma_scale_f32_32x32x64_f8f6f4 v[50:65], v[96:101], v[114:117], v[50:65], v0, v134 op_sel_hi:[0,0,0] cbsz:2 blgp:4
	v_mfma_scale_f32_32x32x64_f8f6f4 v[34:49], v[96:101], v[118:121], v[34:49], v0, v134 op_sel_hi:[0,0,0] cbsz:2 blgp:4
	v_mfma_scale_f32_32x32x64_f8f6f4 v[18:33], v[96:101], v[122:125], v[18:33], v0, v134 op_sel_hi:[0,0,0] cbsz:2 blgp:4
	v_mfma_scale_f32_32x32x64_f8f6f4 v[2:17], v[96:101], v[126:129], v[2:17], v0, v134 op_sel_hi:[0,0,0] cbsz:2 blgp:4
	s_lshl_b32 s4, s34, 8
	s_add_i32 s4, s36, s4
	v_or_b32_e32 v66, s4, v71
	v_lshlrev_b32_e32 v66, 2, v66
	global_load_dword v84, v66, s[0:1]
	global_load_dword v85, v66, s[0:1] offset:128
	global_load_dword v86, v66, s[0:1] offset:256
	global_load_dword v87, v66, s[0:1] offset:384
	s_setprio 0
	s_barrier
	s_cmpk_gt_u32 s33, 0xff
	s_cbranch_scc1 .LBB1_6
	s_barrier
.LBB1_6:
	s_lshl_b32 s4, s34, 8
	s_add_i32 s36, s36, s4
	v_or_b32_e32 v0, s36, v71
	v_mov_b32_e32 v1, 0
	v_lshlrev_b64 v[0:1], 2, v[0:1]
	v_lshl_add_u64 v[66:67], s[0:1], 0, v[0:1]
	s_or_b32 s0, s30, s31
	v_lshlrev_b32_e32 v68, 2, v70
	v_lshl_or_b32 v68, s0, 7, v68
	v_or_b32_e32 v68, s35, v68
	v_ashrrev_i32_e32 v69, 31, v68
	v_lshlrev_b64 v[68:69], 12, v[68:69]
	v_lshl_add_u64 v[68:69], s[2:3], 0, v[68:69]
	s_movk_i32 s1, 0x1000
	v_lshl_add_u64 v[0:1], v[68:69], 0, v[0:1]
	v_add_co_u32_e32 v66, vcc, s1, v0
	s_movk_i32 s4, 0x2000
	s_nop 0
	v_addc_co_u32_e32 v67, vcc, 0, v1, vcc
	v_add_co_u32_e32 v68, vcc, s4, v0
	s_movk_i32 s5, 0x3000
	s_nop 0
	v_addc_co_u32_e32 v69, vcc, 0, v1, vcc
	v_add_co_u32_e32 v70, vcc, s5, v0
	s_mov_b32 s6, 0x8000
	s_nop 0
	v_addc_co_u32_e32 v71, vcc, 0, v1, vcc
	v_add_co_u32_e32 v72, vcc, s6, v0
	s_mov_b32 s7, 0x9000
	s_nop 0
	v_addc_co_u32_e32 v73, vcc, 0, v1, vcc
	v_add_co_u32_e32 v74, vcc, s7, v0
	s_mov_b32 s8, 0xa000
	s_nop 0
	v_addc_co_u32_e32 v75, vcc, 0, v1, vcc
	v_add_co_u32_e32 v76, vcc, s8, v0
	s_mov_b32 s9, 0xb000
	s_nop 0
	v_addc_co_u32_e32 v77, vcc, 0, v1, vcc
	v_add_co_u32_e32 v78, vcc, s9, v0
	s_mov_b32 s10, 0x10000
	s_nop 0
	v_addc_co_u32_e32 v79, vcc, 0, v1, vcc
	v_add_co_u32_e32 v80, vcc, s10, v0
	s_mov_b32 s11, 0x11000
	s_nop 0
	v_addc_co_u32_e32 v81, vcc, 0, v1, vcc
	v_add_co_u32_e32 v82, vcc, s11, v0
	s_mov_b32 s12, 0x12000
	s_nop 0
	v_addc_co_u32_e32 v83, vcc, 0, v1, vcc
	s_mov_b32 s0, 0x13000
	s_waitcnt vmcnt(0)
	v_mul_f32_e32 v34, v85, v34
	v_mul_f32_e32 v50, v84, v50
	v_mul_f32_e32 v51, v84, v51
	v_mul_f32_e32 v52, v84, v52
	v_mul_f32_e32 v53, v84, v53
	v_mul_f32_e32 v54, v84, v54
	v_mul_f32_e32 v55, v84, v55
	v_mul_f32_e32 v56, v84, v56
	v_mul_f32_e32 v57, v84, v57
	v_mul_f32_e32 v58, v84, v58
	v_mul_f32_e32 v59, v84, v59
	global_store_dword v[0:1], v50, off nt
	global_store_dword v[68:69], v51, off offset:-4096 nt
	global_store_dword v[68:69], v52, off nt
	global_store_dword v[70:71], v53, off nt
	global_store_dword v[74:75], v54, off offset:-4096 nt
	global_store_dword v[74:75], v55, off nt
	global_store_dword v[78:79], v56, off offset:-4096 nt
	global_store_dword v[78:79], v57, off nt
	global_store_dword v[82:83], v58, off offset:-4096 nt
	global_store_dword v[82:83], v59, off nt
	v_add_co_u32_e32 v50, vcc, s12, v0
	v_mul_f32_e32 v54, v84, v61
	s_nop 0
	v_addc_co_u32_e32 v51, vcc, 0, v1, vcc
	v_add_co_u32_e32 v52, vcc, s0, v0
	s_mov_b32 s0, 0x18000
	s_nop 0
	v_addc_co_u32_e32 v53, vcc, 0, v1, vcc
	global_store_dword v[52:53], v54, off nt
	v_add_co_u32_e32 v54, vcc, s0, v0
	s_mov_b32 s0, 0x19000
	s_nop 0
	v_addc_co_u32_e32 v55, vcc, 0, v1, vcc
	v_add_co_u32_e32 v56, vcc, s0, v0
	v_mul_f32_e32 v58, v84, v62
	s_nop 0
	v_addc_co_u32_e32 v57, vcc, 0, v1, vcc
	global_store_dword v[56:57], v58, off offset:-4096 nt
	v_mul_f32_e32 v58, v84, v63
	s_mov_b32 s0, 0x1a000
	global_store_dword v[56:57], v58, off nt
	v_add_co_u32_e32 v58, vcc, s0, v0
	v_mul_f32_e32 v60, v84, v60
	s_nop 0
	v_addc_co_u32_e32 v59, vcc, 0, v1, vcc
	s_mov_b32 s0, 0x1b000
	v_mul_f32_e32 v18, v86, v18
	v_mul_f32_e32 v2, v87, v2
	global_store_dword v[52:53], v60, off offset:-4096 nt
	v_add_co_u32_e32 v60, vcc, s0, v0
	global_store_dword v[0:1], v34, off offset:128 nt
	v_mul_f32_e32 v34, v85, v35
	global_store_dword v[0:1], v18, off offset:256 nt
	v_mul_f32_e32 v18, v86, v19
	global_store_dword v[0:1], v2, off offset:384 nt
	v_mul_f32_e32 v0, v87, v3
	global_store_dword v[66:67], v34, off offset:128 nt
	v_mul_f32_e32 v34, v85, v36
	global_store_dword v[66:67], v18, off offset:256 nt
	v_mul_f32_e32 v18, v86, v20
	global_store_dword v[66:67], v0, off offset:384 nt
	v_mul_f32_e32 v0, v87, v4
	global_store_dword v[68:69], v34, off offset:128 nt
	v_mul_f32_e32 v34, v85, v37
	global_store_dword v[68:69], v18, off offset:256 nt
	v_mul_f32_e32 v18, v86, v21
	global_store_dword v[68:69], v0, off offset:384 nt
	v_mul_f32_e32 v0, v87, v5
	global_store_dword v[70:71], v34, off offset:128 nt
	v_mul_f32_e32 v34, v85, v38
	global_store_dword v[70:71], v18, off offset:256 nt
	v_mul_f32_e32 v18, v86, v22
	global_store_dword v[70:71], v0, off offset:384 nt
	v_mul_f32_e32 v0, v87, v6
	global_store_dword v[72:73], v34, off offset:128 nt
	v_mul_f32_e32 v34, v85, v39
	global_store_dword v[72:73], v18, off offset:256 nt
	v_mul_f32_e32 v18, v86, v23
	global_store_dword v[72:73], v0, off offset:384 nt
	v_mul_f32_e32 v0, v87, v7
	global_store_dword v[74:75], v34, off offset:128 nt
	v_mul_f32_e32 v34, v85, v40
	global_store_dword v[74:75], v18, off offset:256 nt
	v_mul_f32_e32 v18, v86, v24
	global_store_dword v[74:75], v0, off offset:384 nt
	v_mul_f32_e32 v0, v87, v8
	global_store_dword v[76:77], v34, off offset:128 nt
	v_mul_f32_e32 v34, v85, v41
	global_store_dword v[76:77], v18, off offset:256 nt
	v_mul_f32_e32 v18, v86, v25
	global_store_dword v[76:77], v0, off offset:384 nt
	v_mul_f32_e32 v0, v87, v9
	global_store_dword v[78:79], v34, off offset:128 nt
	v_mul_f32_e32 v34, v85, v42
	global_store_dword v[78:79], v18, off offset:256 nt
	v_mul_f32_e32 v18, v86, v26
	global_store_dword v[78:79], v0, off offset:384 nt
	v_mul_f32_e32 v0, v87, v10
	global_store_dword v[80:81], v34, off offset:128 nt
	v_mul_f32_e32 v34, v85, v43
	global_store_dword v[80:81], v18, off offset:256 nt
	v_mul_f32_e32 v18, v86, v27
	global_store_dword v[80:81], v0, off offset:384 nt
	v_mul_f32_e32 v0, v87, v11
	global_store_dword v[82:83], v34, off offset:128 nt
	v_mul_f32_e32 v34, v85, v44
	global_store_dword v[82:83], v18, off offset:256 nt
	v_mul_f32_e32 v18, v86, v28
	global_store_dword v[82:83], v0, off offset:384 nt
	v_mul_f32_e32 v0, v87, v12
	global_store_dword v[50:51], v34, off offset:128 nt
	v_mul_f32_e32 v34, v85, v45
	global_store_dword v[50:51], v18, off offset:256 nt
	v_mul_f32_e32 v18, v86, v29
	global_store_dword v[50:51], v0, off offset:384 nt
	v_mul_f32_e32 v0, v87, v13
	global_store_dword v[52:53], v34, off offset:128 nt
	v_mul_f32_e32 v34, v85, v46
	global_store_dword v[52:53], v18, off offset:256 nt
	v_mul_f32_e32 v18, v86, v30
	global_store_dword v[52:53], v0, off offset:384 nt
	v_mul_f32_e32 v0, v87, v14
	global_store_dword v[54:55], v34, off offset:128 nt
	v_mul_f32_e32 v34, v85, v47
	global_store_dword v[54:55], v18, off offset:256 nt
	v_mul_f32_e32 v18, v86, v31
	global_store_dword v[54:55], v0, off offset:384 nt
	v_mul_f32_e32 v0, v87, v15
	v_mul_f32_e32 v62, v84, v64
	v_addc_co_u32_e32 v61, vcc, 0, v1, vcc
	global_store_dword v[56:57], v34, off offset:128 nt
	v_mul_f32_e32 v34, v85, v48
	global_store_dword v[56:57], v18, off offset:256 nt
	v_mul_f32_e32 v18, v86, v32
	global_store_dword v[56:57], v0, off offset:384 nt
	v_mul_f32_e32 v0, v87, v16
	global_store_dword v[60:61], v62, off offset:-4096 nt
	v_mul_f32_e32 v62, v84, v65
	global_store_dword v[58:59], v34, off offset:128 nt
	v_mul_f32_e32 v34, v85, v49
	global_store_dword v[58:59], v18, off offset:256 nt
	v_mul_f32_e32 v18, v86, v33
	global_store_dword v[58:59], v0, off offset:384 nt
	v_mul_f32_e32 v0, v87, v17
	global_store_dword v[60:61], v62, off nt
	global_store_dword v[60:61], v34, off offset:128 nt
	global_store_dword v[60:61], v18, off offset:256 nt
	global_store_dword v[60:61], v0, off offset:384 nt
	s_endpgm
